# mega stack + dense-up group size 4 + N1/final-norm wave sums by DPP and permlane swaps instead of ds_bpermute
# baseline (speedup 1.0000x reference)
; __device__ __forceinline__ unsigned pk2(float lo, float hi) { f32x2 v = {lo, hi}; return __builtin_bit_cast(unsigned, __builtin_convertvector(v, bf2_t)); }
; template <int BIT = 0> __device__ __forceinline__ void st16w(void* p, u32x4 v) { if ((WT_STORES >> BIT) & 1) asm volatile("global_store_dwordx4 %0, %1, off sc1\n\ts_nop 1" :: "v"(p), "v"(v) : "memory"); else *(u32x4*)p = v; }
; template <int KIND, int NR> __device__ __forceinline__ void rows_block(Frame& F, const Args& a, int l, bool combine, bool moe, int m0, const f32x4 (&gm)[2][2], const f32x4 (&shv)[2][2], LAS const float* wr_l, LAS int* lcnt) {
;     ...
;         float ss = 0.f;
; #pragma unroll
;         for (int j = 0; j < 2; ++j)
; #pragma unroll
;             for (int hf = 0; hf < 2; ++hf) { const f32x4 x = v[i][j][hf]; ss += (x[0] * x[0] + x[1] * x[1]) + (x[2] * x[2] + x[3] * x[3]); }
;         ss = wsum(ss, lane);
;         const float r = rsqrtf(ss * (1.f / D) + EPS);
;     ...
;             for (int j = 0; j < 2; ++j) {
;                 const f32x4 y0 = v[i][j][0] * (gm[j][0] * r) + shv[j][0], y1 = v[i][j][1] * (gm[j][1] * r) + shv[j][1];
;                 u32x4 ob; ob.x = pk2(y0[0], y0[1]); ob.y = pk2(y0[2], y0[3]); ob.z = pk2(y1[0], y1[1]); ob.w = pk2(y1[2], y1[3]);
;                 st16w<3>(XN + (size_t)m * D + cbase + 512 * j, ob);
.LBB13_144:
	s_waitcnt vmcnt(2)
	s_nop 0
	v_pk_mul_f32 v[34:35], v[32:33], v[32:33]
	v_pk_mul_f32 v[36:37], v[30:31], v[30:31]
	s_mov_b64 s[22:23], 0
	v_pk_mov_b32 v[38:39], v[36:37], v[34:35] op_sel:[1,0]
	v_mov_b32_e32 v37, v35
	v_pk_add_f32 v[34:35], v[38:39], v[36:37]
	v_pk_mul_f32 v[36:37], v[28:29], v[28:29]
	v_pk_add_f32 v[34:35], v[34:35], v[34:35] op_sel_hi:[0,1]
	v_pk_mul_f32 v[38:39], v[26:27], v[26:27]
	s_waitcnt vmcnt(0)
	v_mul_f32_e32 v34, v22, v22
	v_pk_mov_b32 v[40:41], v[38:39], v[36:37] op_sel:[1,0]
	v_mov_b32_e32 v39, v37
	v_pk_add_f32 v[36:37], v[40:41], v[38:39]
	v_pk_fma_f32 v[38:39], v[22:23], v[22:23], v[34:35] op_sel_hi:[1,1,0]
	v_mul_f32_e32 v34, v24, v24
	v_pk_add_f32 v[36:37], v[36:37], v[36:37] op_sel_hi:[0,1]
	v_pk_fma_f32 v[40:41], v[24:25], v[24:25], v[34:35] op_sel_hi:[1,1,0]
	v_mul_f32_e32 v38, v18, v18
	v_mul_f32_e32 v40, v19, v19
	v_mul_f32_e32 v36, v20, v20
	v_mul_f32_e32 v34, v21, v21
	v_pk_add_f32 v[38:39], v[38:39], v[40:41]
	v_pk_add_f32 v[34:35], v[36:37], v[34:35]
	s_nop 0
	v_pk_add_f32 v[34:35], v[38:39], v[34:35]
	s_nop 0
	v_add_f32_e32 v34, v34, v35
	s_nop 1
	v_mov_b32_dpp v35, v34 quad_perm:[1,0,3,2] row_mask:0xf bank_mask:0xf
	s_waitcnt lgkmcnt(0)
	v_add_f32_e32 v34, v34, v35
	s_nop 1
	v_mov_b32_dpp v35, v34 quad_perm:[2,3,0,1] row_mask:0xf bank_mask:0xf
	s_waitcnt lgkmcnt(0)
	v_add_f32_e32 v34, v34, v35
	s_nop 1
	v_mov_b32_dpp v35, v34 row_half_mirror row_mask:0xf bank_mask:0xf
	s_waitcnt lgkmcnt(0)
	v_add_f32_e32 v34, v34, v35
	s_nop 1
	v_mov_b32_dpp v35, v34 row_mirror row_mask:0xf bank_mask:0xf
	s_waitcnt lgkmcnt(0)
	v_add_f32_e32 v34, v34, v35
	v_mov_b32_e32 v35, v34
	s_nop 1
	v_permlane16_swap_b32_e32 v35, v34
	s_waitcnt lgkmcnt(0)
	v_add_f32_e32 v34, v34, v35
	v_mov_b32_e32 v35, v34
	s_nop 1
	v_permlane32_swap_b32_e32 v35, v34
	s_waitcnt lgkmcnt(0)
	v_add_f32_e32 v34, v34, v35
	v_fmamk_f32 v34, v34, 0x3a800000, v234
	v_cmp_gt_f32_e32 vcc, s93, v34
	v_mul_f32_e32 v35, 0x4b800000, v34
	s_nop 0
	v_cndmask_b32_e32 v34, v34, v35, vcc
	v_rsq_f32_e32 v34, v34
	s_nop 0
	v_mul_f32_e32 v35, 0x45800000, v34
	v_cndmask_b32_e32 v34, v34, v35, vcc
	v_pk_mul_f32 v[36:37], v[214:215], v[34:35] op_sel_hi:[1,0]
	v_pk_mul_f32 v[38:39], v[212:213], v[34:35] op_sel_hi:[1,0]
	v_pk_fma_f32 v[30:31], v[36:37], v[30:31], v[6:7]
	v_pk_fma_f32 v[32:33], v[38:39], v[32:33], v[8:9]
	v_pk_mul_f32 v[36:37], v[198:199], v[34:35] op_sel_hi:[1,0]
	v_pk_mul_f32 v[38:39], v[196:197], v[34:35] op_sel_hi:[1,0]
	s_nop 0
	v_pk_fma_f32 v[38:39], v[38:39], v[28:29], v[4:5]
	v_pk_fma_f32 v[28:29], v[36:37], v[26:27], v[2:3]
	v_cvt_pk_bf16_f32 v26, v30, v31
	v_cvt_pk_bf16_f32 v27, v32, v33
	v_cvt_pk_bf16_f32 v28, v28, v29
	v_cvt_pk_bf16_f32 v29, v38, v39
	global_store_dwordx4 v[192:193], v[26:29], off
	s_nop 1
	v_pk_mul_f32 v[26:27], v[218:219], v[34:35] op_sel_hi:[1,0]
	v_pk_mul_f32 v[28:29], v[216:217], v[34:35] op_sel_hi:[1,0]
	v_pk_fma_f32 v[22:23], v[26:27], v[22:23], v[14:15]
	v_pk_fma_f32 v[24:25], v[28:29], v[24:25], v[16:17]
	v_pk_mul_f32 v[26:27], v[210:211], v[34:35] op_sel_hi:[1,0]
	v_pk_mul_f32 v[28:29], v[208:209], v[34:35] op_sel_hi:[1,0]
	s_nop 0
	v_pk_fma_f32 v[28:29], v[28:29], v[20:21], v[12:13]
	v_pk_fma_f32 v[20:21], v[26:27], v[18:19], v[10:11]
	v_cvt_pk_bf16_f32 v18, v22, v23
	v_cvt_pk_bf16_f32 v19, v24, v25
	v_cvt_pk_bf16_f32 v20, v20, v21
	v_cvt_pk_bf16_f32 v21, v28, v29
	global_store_dwordx4 v[192:193], v[18:21], off offset:1024

; __device__ __forceinline__ unsigned pk2(float lo, float hi) { f32x2 v = {lo, hi}; return __builtin_bit_cast(unsigned, __builtin_convertvector(v, bf2_t)); }
; template <int BIT = 0> __device__ __forceinline__ void st16w(void* p, u32x4 v) { if ((WT_STORES >> BIT) & 1) asm volatile("global_store_dwordx4 %0, %1, off sc1\n\ts_nop 1" :: "v"(p), "v"(v) : "memory"); else *(u32x4*)p = v; }
; template <int KIND, int NR> __device__ __forceinline__ void rows_block(Frame& F, const Args& a, int l, bool combine, bool moe, int m0, const f32x4 (&gm)[2][2], const f32x4 (&shv)[2][2], LAS const float* wr_l, LAS int* lcnt) {
;     ...
;         float ss = 0.f;
; #pragma unroll
;         for (int j = 0; j < 2; ++j)
; #pragma unroll
;             for (int hf = 0; hf < 2; ++hf) { const f32x4 x = v[i][j][hf]; ss += (x[0] * x[0] + x[1] * x[1]) + (x[2] * x[2] + x[3] * x[3]); }
;         ss = wsum(ss, lane);
;         const float r = rsqrtf(ss * (1.f / D) + EPS);
;         if (KIND == 2) {
; #pragma unroll
;             for (int j = 0; j < 2; ++j) { *(f32x4*)((a.out + F.zo) + (size_t)m * D + cbase + 512 * j) = v[i][j][0] * r * gm[j][0]; *(f32x4*)((a.out + F.zo) + (size_t)m * D + cbase + 512 * j + 4) = v[i][j][1] * r * gm[j][1]; }
;         } else {
;             float lg[NE];
; #pragma unroll
;             for (int e = 0; e < NE; ++e) lg[e] = 0.f;
; #pragma unroll
;             for (int j = 0; j < 2; ++j) {
;                 const f32x4 y0 = v[i][j][0] * (gm[j][0] * r) + shv[j][0], y1 = v[i][j][1] * (gm[j][1] * r) + shv[j][1];
;                 u32x4 ob; ob.x = pk2(y0[0], y0[1]); ob.y = pk2(y0[2], y0[3]); ob.z = pk2(y1[0], y1[1]); ob.w = pk2(y1[2], y1[3]);
;                 st16w<3>(XN + (size_t)m * D + cbase + 512 * j, ob);
.LBB13_148:
	s_waitcnt vmcnt(2)
	v_pk_mul_f32 v[82:83], v[48:49], v[48:49]
	v_pk_mul_f32 v[84:85], v[46:47], v[46:47]
	s_mov_b32 s6, 0x358637bd
	v_pk_mov_b32 v[86:87], v[84:85], v[82:83] op_sel:[1,0]
	v_mov_b32_e32 v85, v83
	v_pk_add_f32 v[82:83], v[86:87], v[84:85]
	v_pk_mul_f32 v[84:85], v[44:45], v[44:45]
	v_pk_mul_f32 v[86:87], v[42:43], v[42:43]
	v_pk_add_f32 v[82:83], v[82:83], v[82:83] op_sel:[0,1] op_sel_hi:[1,0]
	v_pk_mov_b32 v[88:89], v[86:87], v[84:85] op_sel:[1,0]
	v_mov_b32_e32 v87, v85
	v_pk_add_f32 v[84:85], v[88:89], v[86:87]
	s_waitcnt vmcnt(1)
	v_mul_f32_e32 v86, v34, v34
	v_mul_f32_e32 v87, v35, v35
	v_pk_add_f32 v[84:85], v[84:85], v[84:85] op_sel:[0,1] op_sel_hi:[1,0]
	v_mov_b32_e32 v83, v86
	v_mov_b32_e32 v85, v87
	v_pk_add_f32 v[82:83], v[82:83], v[84:85]
	s_waitcnt vmcnt(0)
	v_mul_f32_e32 v84, v39, v39
	v_mul_f32_e32 v86, v41, v41
	v_mul_f32_e32 v88, v36, v36
	v_mul_f32_e32 v89, v37, v37
	v_pk_fma_f32 v[84:85], v[38:39], v[38:39], v[84:85] op_sel_hi:[1,1,0]
	v_pk_fma_f32 v[86:87], v[40:41], v[40:41], v[86:87] op_sel_hi:[1,1,0]
	v_mov_b32_e32 v85, v88
	v_mov_b32_e32 v87, v89
	v_pk_add_f32 v[84:85], v[84:85], v[86:87]
	v_pk_mul_f32 v[86:87], v[30:31], v[30:31]
	v_pk_add_f32 v[82:83], v[82:83], v[84:85]
	v_pk_mul_f32 v[84:85], v[32:33], v[32:33]
	s_add_i32 s48, s48, 4
	v_pk_mov_b32 v[88:89], v[86:87], v[84:85] op_sel:[1,0]
	v_mov_b32_e32 v87, v85
	v_pk_add_f32 v[84:85], v[88:89], v[86:87]
	v_pk_mul_f32 v[86:87], v[28:29], v[28:29]
	v_pk_mul_f32 v[88:89], v[26:27], v[26:27]
	v_pk_add_f32 v[84:85], v[84:85], v[84:85] op_sel:[0,1] op_sel_hi:[1,0]
	v_pk_mov_b32 v[90:91], v[88:89], v[86:87] op_sel:[1,0]
	v_mov_b32_e32 v89, v87
	v_pk_add_f32 v[86:87], v[90:91], v[88:89]
	v_mul_f32_e32 v88, v18, v18
	v_mul_f32_e32 v89, v19, v19
	v_pk_add_f32 v[86:87], v[86:87], v[86:87] op_sel:[0,1] op_sel_hi:[1,0]
	v_mov_b32_e32 v85, v88
	v_mov_b32_e32 v87, v89
	v_pk_add_f32 v[84:85], v[84:85], v[86:87]
	v_mul_f32_e32 v86, v23, v23
	v_mul_f32_e32 v88, v25, v25
	v_mul_f32_e32 v90, v20, v20
	v_mul_f32_e32 v91, v21, v21
	v_pk_fma_f32 v[86:87], v[22:23], v[22:23], v[86:87] op_sel_hi:[1,1,0]
	v_pk_fma_f32 v[88:89], v[24:25], v[24:25], v[88:89] op_sel_hi:[1,1,0]
	v_mov_b32_e32 v87, v90
	v_mov_b32_e32 v89, v91
	v_pk_add_f32 v[86:87], v[86:87], v[88:89]
	s_add_i32 s22, s22, 8
	v_pk_add_f32 v[84:85], v[84:85], v[86:87]
	v_mov_b32_e32 v87, v82
	v_mov_b32_e32 v86, v84
	v_mov_b32_e32 v82, v85
	v_pk_add_f32 v[82:83], v[86:87], v[82:83]
	s_nop 1
	v_mov_b32_dpp v85, v83 quad_perm:[1,0,3,2] row_mask:0xf bank_mask:0xf
	s_nop 1
	v_mov_b32_dpp v84, v82 quad_perm:[1,0,3,2] row_mask:0xf bank_mask:0xf
	s_cmp_ge_i32 s48, s2
	s_waitcnt lgkmcnt(0)
	v_pk_add_f32 v[82:83], v[82:83], v[84:85]
	s_nop 1
	v_mov_b32_dpp v85, v83 quad_perm:[2,3,0,1] row_mask:0xf bank_mask:0xf
	s_nop 1
	v_mov_b32_dpp v84, v82 quad_perm:[2,3,0,1] row_mask:0xf bank_mask:0xf
	s_waitcnt lgkmcnt(0)
	v_pk_add_f32 v[82:83], v[82:83], v[84:85]
	s_nop 1
	v_mov_b32_dpp v85, v83 row_half_mirror row_mask:0xf bank_mask:0xf
	s_nop 1
	v_mov_b32_dpp v84, v82 row_half_mirror row_mask:0xf bank_mask:0xf
	s_waitcnt lgkmcnt(0)
	v_pk_add_f32 v[82:83], v[82:83], v[84:85]
	s_nop 1
	v_mov_b32_dpp v85, v83 row_mirror row_mask:0xf bank_mask:0xf
	s_nop 1
	v_mov_b32_dpp v84, v82 row_mirror row_mask:0xf bank_mask:0xf
	s_waitcnt lgkmcnt(0)
	v_pk_add_f32 v[82:83], v[82:83], v[84:85]
	v_mov_b32_e32 v85, v83
	s_nop 1
	v_permlane16_swap_b32_e32 v85, v83
	v_mov_b32_e32 v84, v82
	s_nop 1
	v_permlane16_swap_b32_e32 v84, v82
	s_waitcnt lgkmcnt(0)
	v_pk_add_f32 v[82:83], v[82:83], v[84:85]
	v_mov_b32_e32 v85, v83
	s_nop 1
	v_permlane32_swap_b32_e32 v85, v83
	v_mov_b32_e32 v84, v82
	s_nop 1
	v_permlane32_swap_b32_e32 v84, v82
	s_waitcnt lgkmcnt(0)
	v_pk_add_f32 v[84:85], v[82:83], v[84:85]
	v_mov_b64_e32 v[82:83], s[6:7]
	v_pk_fma_f32 v[84:85], v[84:85], s[92:93], v[82:83] op_sel_hi:[1,0,0]
	s_nop 0
	v_mul_f32_e32 v86, 0x4b800000, v85
	v_cmp_gt_f32_e32 vcc, s93, v85
	s_nop 1
	v_cndmask_b32_e32 v85, v85, v86, vcc
	v_rsq_f32_e32 v85, v85
	v_lshl_add_u64 v[86:87], v[194:195], 0, s[30:31]
	v_mul_f32_e32 v88, 0x45800000, v85
	v_cndmask_b32_e32 v88, v85, v88, vcc
	v_pk_mul_f32 v[90:91], v[214:215], v[88:89] op_sel_hi:[1,0]
	v_pk_mul_f32 v[92:93], v[212:213], v[88:89] op_sel_hi:[1,0]
	v_pk_fma_f32 v[46:47], v[46:47], v[90:91], v[6:7]
	v_pk_fma_f32 v[48:49], v[48:49], v[92:93], v[8:9]
	v_pk_mul_f32 v[90:91], v[198:199], v[88:89] op_sel_hi:[1,0]
	v_pk_mul_f32 v[92:93], v[196:197], v[88:89] op_sel_hi:[1,0]
	v_cmp_gt_f32_e32 vcc, s93, v84
	v_pk_fma_f32 v[92:93], v[44:45], v[92:93], v[4:5]
	v_pk_fma_f32 v[44:45], v[42:43], v[90:91], v[2:3]
	v_cvt_pk_bf16_f32 v42, v46, v47
	v_cvt_pk_bf16_f32 v43, v48, v49
	v_cvt_pk_bf16_f32 v44, v44, v45
	v_cvt_pk_bf16_f32 v45, v92, v93
	global_store_dwordx4 v[86:87], v[42:45], off
	s_nop 1
	v_pk_mul_f32 v[42:43], v[218:219], v[88:89] op_sel_hi:[1,0]
	v_pk_mul_f32 v[44:45], v[216:217], v[88:89] op_sel_hi:[1,0]
	v_pk_fma_f32 v[38:39], v[38:39], v[42:43], v[14:15]
	v_pk_fma_f32 v[40:41], v[40:41], v[44:45], v[16:17]
	v_pk_mul_f32 v[42:43], v[210:211], v[88:89] op_sel_hi:[1,0]
	v_pk_mul_f32 v[44:45], v[208:209], v[88:89] op_sel_hi:[1,0]
	s_nop 0
	v_pk_fma_f32 v[44:45], v[36:37], v[44:45], v[12:13]
	v_pk_fma_f32 v[36:37], v[34:35], v[42:43], v[10:11]
	v_cvt_pk_bf16_f32 v34, v38, v39
	v_mul_f32_e32 v38, 0x4b800000, v84
	v_cndmask_b32_e32 v38, v84, v38, vcc
	v_rsq_f32_e32 v38, v38
	v_cvt_pk_bf16_f32 v35, v40, v41
	v_cvt_pk_bf16_f32 v36, v36, v37
	v_cvt_pk_bf16_f32 v37, v44, v45
	global_store_dwordx4 v[86:87], v[34:37], off offset:1024
	v_pk_mul_f32 v[40:41], v[62:63], v[62:63]
	s_nop 0
	v_mul_f32_e32 v34, 0x45800000, v38
; __device__ __forceinline__ unsigned pk2(float lo, float hi) { f32x2 v = {lo, hi}; return __builtin_bit_cast(unsigned, __builtin_convertvector(v, bf2_t)); }
; template <int BIT = 0> __device__ __forceinline__ void st16w(void* p, u32x4 v) { if ((WT_STORES >> BIT) & 1) asm volatile("global_store_dwordx4 %0, %1, off sc1\n\ts_nop 1" :: "v"(p), "v"(v) : "memory"); else *(u32x4*)p = v; }
; template <int KIND, int NR> __device__ __forceinline__ void rows_block(Frame& F, const Args& a, int l, bool combine, bool moe, int m0, const f32x4 (&gm)[2][2], const f32x4 (&shv)[2][2], LAS const float* wr_l, LAS int* lcnt) {
;     ...
;         float ss = 0.f;
; #pragma unroll
;         for (int j = 0; j < 2; ++j)
; #pragma unroll
;             for (int hf = 0; hf < 2; ++hf) { const f32x4 x = v[i][j][hf]; ss += (x[0] * x[0] + x[1] * x[1]) + (x[2] * x[2] + x[3] * x[3]); }
;         ss = wsum(ss, lane);
;         const float r = rsqrtf(ss * (1.f / D) + EPS);
;         if (KIND == 2) {
; #pragma unroll
;             for (int j = 0; j < 2; ++j) { *(f32x4*)((a.out + F.zo) + (size_t)m * D + cbase + 512 * j) = v[i][j][0] * r * gm[j][0]; *(f32x4*)((a.out + F.zo) + (size_t)m * D + cbase + 512 * j + 4) = v[i][j][1] * r * gm[j][1]; }
;         } else {
;             float lg[NE];
; #pragma unroll
;             for (int e = 0; e < NE; ++e) lg[e] = 0.f;
; #pragma unroll
;             for (int j = 0; j < 2; ++j) {
;                 const f32x4 y0 = v[i][j][0] * (gm[j][0] * r) + shv[j][0], y1 = v[i][j][1] * (gm[j][1] * r) + shv[j][1];
;                 u32x4 ob; ob.x = pk2(y0[0], y0[1]); ob.y = pk2(y0[2], y0[3]); ob.z = pk2(y1[0], y1[1]); ob.w = pk2(y1[2], y1[3]);
;                 st16w<3>(XN + (size_t)m * D + cbase + 512 * j, ob);
	v_cndmask_b32_e32 v34, v38, v34, vcc
	v_pk_mul_f32 v[38:39], v[64:65], v[64:65]
	v_mul_f32_e32 v35, v54, v54
	v_pk_mov_b32 v[42:43], v[40:41], v[38:39] op_sel:[1,0]
	v_mov_b32_e32 v41, v39
	v_pk_add_f32 v[38:39], v[42:43], v[40:41]
	v_pk_mul_f32 v[40:41], v[52:53], v[52:53]
	v_pk_mul_f32 v[42:43], v[50:51], v[50:51]
	v_pk_add_f32 v[38:39], v[38:39], v[38:39] op_sel:[0,1] op_sel_hi:[1,0]
	v_pk_mov_b32 v[44:45], v[42:43], v[40:41] op_sel:[1,0]
	v_mov_b32_e32 v43, v41
	v_pk_add_f32 v[40:41], v[44:45], v[42:43]
	v_mul_f32_e32 v42, v55, v55
	v_pk_add_f32 v[40:41], v[40:41], v[40:41] op_sel:[0,1] op_sel_hi:[1,0]
	v_mov_b32_e32 v39, v35
	v_mov_b32_e32 v41, v42
	v_pk_add_f32 v[38:39], v[38:39], v[40:41]
	v_mul_f32_e32 v40, v59, v59
	v_mul_f32_e32 v43, v56, v56
	v_pk_fma_f32 v[40:41], v[58:59], v[58:59], v[40:41] op_sel_hi:[1,1,0]
	v_mul_f32_e32 v42, v61, v61
	v_mul_f32_e32 v44, v57, v57
	v_mov_b32_e32 v41, v43
	v_pk_fma_f32 v[42:43], v[60:61], v[60:61], v[42:43] op_sel_hi:[1,1,0]
	v_mul_f32_e32 v35, v70, v70
	v_mov_b32_e32 v43, v44
	v_pk_add_f32 v[40:41], v[40:41], v[42:43]
	v_pk_mul_f32 v[42:43], v[78:79], v[78:79]
	v_pk_add_f32 v[38:39], v[38:39], v[40:41]
	v_pk_mul_f32 v[40:41], v[80:81], v[80:81]
	v_lshl_add_u64 v[36:37], v[194:195], 0, s[36:37]
	v_pk_mov_b32 v[44:45], v[42:43], v[40:41] op_sel:[1,0]
	v_mov_b32_e32 v43, v41
	v_pk_add_f32 v[40:41], v[44:45], v[42:43]
	v_pk_mul_f32 v[42:43], v[68:69], v[68:69]
	v_pk_mul_f32 v[44:45], v[66:67], v[66:67]
	v_pk_add_f32 v[40:41], v[40:41], v[40:41] op_sel:[0,1] op_sel_hi:[1,0]
	v_pk_mov_b32 v[46:47], v[44:45], v[42:43] op_sel:[1,0]
	v_mov_b32_e32 v45, v43
	v_pk_add_f32 v[42:43], v[46:47], v[44:45]
	v_mul_f32_e32 v44, v71, v71
	v_pk_add_f32 v[42:43], v[42:43], v[42:43] op_sel:[0,1] op_sel_hi:[1,0]
	v_mov_b32_e32 v41, v35
	v_mov_b32_e32 v43, v44
	v_pk_add_f32 v[40:41], v[40:41], v[42:43]
	v_mul_f32_e32 v42, v75, v75
	v_mul_f32_e32 v45, v72, v72
	v_pk_fma_f32 v[42:43], v[74:75], v[74:75], v[42:43] op_sel_hi:[1,1,0]
	v_mul_f32_e32 v44, v77, v77
	v_mul_f32_e32 v46, v73, v73
	v_mov_b32_e32 v43, v45
	v_pk_fma_f32 v[44:45], v[76:77], v[76:77], v[44:45] op_sel_hi:[1,1,0]
	s_nop 0
	v_mov_b32_e32 v45, v46
	v_pk_add_f32 v[42:43], v[42:43], v[44:45]
	v_pk_mul_f32 v[44:45], v[212:213], v[34:35] op_sel_hi:[1,0]
	v_pk_add_f32 v[40:41], v[40:41], v[42:43]
	v_mov_b32_e32 v43, v38
	v_mov_b32_e32 v42, v40
	v_mov_b32_e32 v38, v41
	v_pk_add_f32 v[38:39], v[42:43], v[38:39]
	s_nop 1
	v_mov_b32_dpp v41, v39 quad_perm:[1,0,3,2] row_mask:0xf bank_mask:0xf
	s_nop 1
	v_mov_b32_dpp v40, v38 quad_perm:[1,0,3,2] row_mask:0xf bank_mask:0xf
	v_pk_mul_f32 v[42:43], v[214:215], v[34:35] op_sel_hi:[1,0]
	v_pk_fma_f32 v[32:33], v[32:33], v[44:45], v[8:9]
	v_pk_fma_f32 v[30:31], v[30:31], v[42:43], v[6:7]
	v_pk_mul_f32 v[42:43], v[198:199], v[34:35] op_sel_hi:[1,0]
	s_waitcnt lgkmcnt(0)
	v_pk_add_f32 v[38:39], v[38:39], v[40:41]
	s_nop 1
	v_mov_b32_dpp v41, v39 quad_perm:[2,3,0,1] row_mask:0xf bank_mask:0xf
	s_nop 1
	v_mov_b32_dpp v40, v38 quad_perm:[2,3,0,1] row_mask:0xf bank_mask:0xf
	v_pk_mul_f32 v[44:45], v[196:197], v[34:35] op_sel_hi:[1,0]
	s_waitcnt lgkmcnt(0)
	v_pk_add_f32 v[38:39], v[38:39], v[40:41]
	s_nop 1
	v_mov_b32_dpp v41, v39 row_half_mirror row_mask:0xf bank_mask:0xf
	s_nop 1
	v_mov_b32_dpp v40, v38 row_half_mirror row_mask:0xf bank_mask:0xf
	v_pk_fma_f32 v[44:45], v[28:29], v[44:45], v[4:5]
	v_pk_fma_f32 v[28:29], v[26:27], v[42:43], v[2:3]
	v_cvt_pk_bf16_f32 v26, v30, v31
	v_cvt_pk_bf16_f32 v27, v32, v33
	s_waitcnt lgkmcnt(0)
	v_pk_add_f32 v[30:31], v[38:39], v[40:41]
	s_nop 1
	v_mov_b32_dpp v33, v31 row_mirror row_mask:0xf bank_mask:0xf
	s_nop 1
	v_mov_b32_dpp v32, v30 row_mirror row_mask:0xf bank_mask:0xf
	v_cvt_pk_bf16_f32 v28, v28, v29
	v_cvt_pk_bf16_f32 v29, v44, v45
	global_store_dwordx4 v[36:37], v[26:29], off
	s_nop 1
	v_pk_mul_f32 v[28:29], v[216:217], v[34:35] op_sel_hi:[1,0]
	v_pk_mul_f32 v[26:27], v[218:219], v[34:35] op_sel_hi:[1,0]
	v_pk_fma_f32 v[24:25], v[24:25], v[28:29], v[16:17]
	s_waitcnt lgkmcnt(0)
; __device__ __forceinline__ unsigned pk2(float lo, float hi) { f32x2 v = {lo, hi}; return __builtin_bit_cast(unsigned, __builtin_convertvector(v, bf2_t)); }
; template <int BIT = 0> __device__ __forceinline__ void st16w(void* p, u32x4 v) { if ((WT_STORES >> BIT) & 1) asm volatile("global_store_dwordx4 %0, %1, off sc1\n\ts_nop 1" :: "v"(p), "v"(v) : "memory"); else *(u32x4*)p = v; }
; template <int KIND, int NR> __device__ __forceinline__ void rows_block(Frame& F, const Args& a, int l, bool combine, bool moe, int m0, const f32x4 (&gm)[2][2], const f32x4 (&shv)[2][2], LAS const float* wr_l, LAS int* lcnt) {
;     ...
;         float ss = 0.f;
; #pragma unroll
;         for (int j = 0; j < 2; ++j)
; #pragma unroll
;             for (int hf = 0; hf < 2; ++hf) { const f32x4 x = v[i][j][hf]; ss += (x[0] * x[0] + x[1] * x[1]) + (x[2] * x[2] + x[3] * x[3]); }
;         ss = wsum(ss, lane);
;         const float r = rsqrtf(ss * (1.f / D) + EPS);
;         if (KIND == 2) {
; #pragma unroll
;             for (int j = 0; j < 2; ++j) { *(f32x4*)((a.out + F.zo) + (size_t)m * D + cbase + 512 * j) = v[i][j][0] * r * gm[j][0]; *(f32x4*)((a.out + F.zo) + (size_t)m * D + cbase + 512 * j + 4) = v[i][j][1] * r * gm[j][1]; }
;         } else {
;             float lg[NE];
; #pragma unroll
;             for (int e = 0; e < NE; ++e) lg[e] = 0.f;
; #pragma unroll
;             for (int j = 0; j < 2; ++j) {
;                 const f32x4 y0 = v[i][j][0] * (gm[j][0] * r) + shv[j][0], y1 = v[i][j][1] * (gm[j][1] * r) + shv[j][1];
;                 u32x4 ob; ob.x = pk2(y0[0], y0[1]); ob.y = pk2(y0[2], y0[3]); ob.z = pk2(y1[0], y1[1]); ob.w = pk2(y1[2], y1[3]);
;                 st16w<3>(XN + (size_t)m * D + cbase + 512 * j, ob);
	v_pk_add_f32 v[28:29], v[30:31], v[32:33]
	v_mov_b32_e32 v31, v29
	s_nop 1
	v_permlane16_swap_b32_e32 v31, v29
	v_mov_b32_e32 v30, v28
	s_nop 1
	v_permlane16_swap_b32_e32 v30, v28
	v_pk_fma_f32 v[22:23], v[22:23], v[26:27], v[14:15]
	v_pk_mul_f32 v[26:27], v[210:211], v[34:35] op_sel_hi:[1,0]
	v_pk_mul_f32 v[32:33], v[208:209], v[34:35] op_sel_hi:[1,0]
	s_waitcnt lgkmcnt(0)
	v_pk_add_f32 v[28:29], v[28:29], v[30:31]
	v_mov_b32_e32 v31, v29
	s_nop 1
	v_permlane32_swap_b32_e32 v31, v29
	v_mov_b32_e32 v30, v28
	s_nop 1
	v_permlane32_swap_b32_e32 v30, v28
	v_pk_fma_f32 v[32:33], v[20:21], v[32:33], v[12:13]
	v_pk_fma_f32 v[20:21], v[18:19], v[26:27], v[10:11]
	v_cvt_pk_bf16_f32 v18, v22, v23
	v_cvt_pk_bf16_f32 v20, v20, v21
	s_waitcnt lgkmcnt(0)
	v_pk_add_f32 v[22:23], v[28:29], v[30:31]
	v_cvt_pk_bf16_f32 v19, v24, v25
	v_pk_fma_f32 v[22:23], v[22:23], s[92:93], v[82:83] op_sel_hi:[1,0,0]
	v_lshl_add_u64 v[24:25], v[194:195], 0, s[34:35]
	v_mul_f32_e32 v21, 0x4b800000, v23
	v_cmp_gt_f32_e32 vcc, s93, v23
	s_nop 1
	v_cndmask_b32_e32 v21, v23, v21, vcc
	v_rsq_f32_e32 v23, v21
	v_cvt_pk_bf16_f32 v21, v32, v33
	global_store_dwordx4 v[36:37], v[18:21], off offset:1024
	s_nop 1
	v_mul_f32_e32 v18, 0x45800000, v23
	v_cndmask_b32_e32 v26, v23, v18, vcc
	v_pk_mul_f32 v[18:19], v[214:215], v[26:27] op_sel_hi:[1,0]
	v_pk_mul_f32 v[20:21], v[212:213], v[26:27] op_sel_hi:[1,0]
	v_pk_mul_f32 v[28:29], v[198:199], v[26:27] op_sel_hi:[1,0]
	v_pk_mul_f32 v[30:31], v[196:197], v[26:27] op_sel_hi:[1,0]
	v_pk_fma_f32 v[20:21], v[64:65], v[20:21], v[8:9]
	v_pk_fma_f32 v[18:19], v[62:63], v[18:19], v[6:7]
	v_pk_fma_f32 v[30:31], v[52:53], v[30:31], v[4:5]
	v_pk_fma_f32 v[28:29], v[50:51], v[28:29], v[2:3]
	v_cvt_pk_bf16_f32 v18, v18, v19
	v_cvt_pk_bf16_f32 v19, v20, v21
	v_cvt_pk_bf16_f32 v20, v28, v29
	v_cvt_pk_bf16_f32 v21, v30, v31
	global_store_dwordx4 v[24:25], v[18:21], off
	v_cmp_gt_f32_e32 vcc, s93, v22
	v_pk_mul_f32 v[28:29], v[210:211], v[26:27] op_sel_hi:[1,0]
	v_pk_mul_f32 v[18:19], v[218:219], v[26:27] op_sel_hi:[1,0]
	v_pk_mul_f32 v[20:21], v[216:217], v[26:27] op_sel_hi:[1,0]
	v_pk_fma_f32 v[18:19], v[58:59], v[18:19], v[14:15]
	v_pk_fma_f32 v[20:21], v[60:61], v[20:21], v[16:17]
	v_cvt_pk_bf16_f32 v18, v18, v19
	v_cvt_pk_bf16_f32 v19, v20, v21
	v_mul_f32_e32 v20, 0x4b800000, v22
	v_cndmask_b32_e32 v20, v22, v20, vcc
	v_rsq_f32_e32 v22, v20
	v_pk_mul_f32 v[26:27], v[208:209], v[26:27] op_sel_hi:[1,0]
	v_pk_fma_f32 v[28:29], v[54:55], v[28:29], v[10:11]
	v_pk_fma_f32 v[26:27], v[56:57], v[26:27], v[12:13]
	v_cvt_pk_bf16_f32 v20, v28, v29
	v_cvt_pk_bf16_f32 v21, v26, v27
	global_store_dwordx4 v[24:25], v[18:21], off offset:1024
	v_lshl_add_u64 v[24:25], v[194:195], 0, s[40:41]
	s_nop 0
	v_mul_f32_e32 v18, 0x45800000, v22
	v_cndmask_b32_e32 v22, v22, v18, vcc
	v_pk_mul_f32 v[18:19], v[214:215], v[22:23] op_sel_hi:[1,0]
	v_pk_mul_f32 v[20:21], v[212:213], v[22:23] op_sel_hi:[1,0]
	v_pk_mul_f32 v[26:27], v[198:199], v[22:23] op_sel_hi:[1,0]
	v_pk_mul_f32 v[28:29], v[196:197], v[22:23] op_sel_hi:[1,0]
	v_pk_fma_f32 v[20:21], v[80:81], v[20:21], v[8:9]
	v_pk_fma_f32 v[18:19], v[78:79], v[18:19], v[6:7]
	v_pk_fma_f32 v[28:29], v[68:69], v[28:29], v[4:5]
	v_pk_fma_f32 v[26:27], v[66:67], v[26:27], v[2:3]
	v_cvt_pk_bf16_f32 v18, v18, v19
	v_cvt_pk_bf16_f32 v19, v20, v21
	v_cvt_pk_bf16_f32 v20, v26, v27
	v_cvt_pk_bf16_f32 v21, v28, v29
	global_store_dwordx4 v[24:25], v[18:21], off
	v_pk_mul_f32 v[26:27], v[210:211], v[22:23] op_sel_hi:[1,0]
	s_nop 0
	v_pk_mul_f32 v[18:19], v[218:219], v[22:23] op_sel_hi:[1,0]
	v_pk_mul_f32 v[20:21], v[216:217], v[22:23] op_sel_hi:[1,0]
	v_pk_mul_f32 v[22:23], v[208:209], v[22:23] op_sel_hi:[1,0]
	v_pk_fma_f32 v[20:21], v[76:77], v[20:21], v[16:17]
	v_pk_fma_f32 v[18:19], v[74:75], v[18:19], v[14:15]
	v_pk_fma_f32 v[22:23], v[72:73], v[22:23], v[12:13]
	v_pk_fma_f32 v[26:27], v[70:71], v[26:27], v[10:11]
	v_cvt_pk_bf16_f32 v18, v18, v19
	v_cvt_pk_bf16_f32 v19, v20, v21
	v_cvt_pk_bf16_f32 v20, v26, v27
	v_cvt_pk_bf16_f32 v21, v22, v23
	global_store_dwordx4 v[24:25], v[18:21], off offset:1024
	s_cbranch_scc1 .LBB13_136

; template <int KIND, int NR> __device__ __forceinline__ void rows_block(Frame& F, const Args& a, int l, bool combine, bool moe, int m0, const f32x4 (&gm)[2][2], const f32x4 (&shv)[2][2], LAS const float* wr_l, LAS int* lcnt) {
;     ...
;         float ss = 0.f;
; #pragma unroll
;         for (int j = 0; j < 2; ++j)
; #pragma unroll
;             for (int hf = 0; hf < 2; ++hf) { const f32x4 x = v[i][j][hf]; ss += (x[0] * x[0] + x[1] * x[1]) + (x[2] * x[2] + x[3] * x[3]); }
;         ss = wsum(ss, lane);
;         const float r = rsqrtf(ss * (1.f / D) + EPS);
;         if (KIND == 2) {
; #pragma unroll
;             for (int j = 0; j < 2; ++j) { *(f32x4*)((a.out + F.zo) + (size_t)m * D + cbase + 512 * j) = v[i][j][0] * r * gm[j][0]; *(f32x4*)((a.out + F.zo) + (size_t)m * D + cbase + 512 * j + 4) = v[i][j][1] * r * gm[j][1]; }
.LBB13_1633:
	v_pk_mul_f32 v[16:17], v[142:143], v[142:143]
	v_pk_mul_f32 v[18:19], v[140:141], v[140:141]
	s_lshl_b64 s[0:1], s[18:19], 12
	v_pk_mov_b32 v[20:21], v[18:19], v[16:17] op_sel:[1,0]
	v_mov_b32_e32 v19, v17
	v_pk_add_f32 v[16:17], v[20:21], v[18:19]
	v_pk_mul_f32 v[18:19], v[138:139], v[138:139]
	v_pk_mul_f32 v[20:21], v[136:137], v[136:137]
	v_pk_add_f32 v[16:17], v[16:17], v[16:17] op_sel:[0,1] op_sel_hi:[1,0]
	v_pk_mov_b32 v[22:23], v[20:21], v[18:19] op_sel:[1,0]
	v_mov_b32_e32 v21, v19
	v_pk_add_f32 v[18:19], v[22:23], v[20:21]
	v_mul_f32_e32 v20, v130, v130
	v_mul_f32_e32 v21, v131, v131
	v_pk_add_f32 v[18:19], v[18:19], v[18:19] op_sel:[0,1] op_sel_hi:[1,0]
	v_mov_b32_e32 v17, v20
	v_mov_b32_e32 v19, v21
	v_pk_add_f32 v[16:17], v[16:17], v[18:19]
	v_mul_f32_e32 v18, v133, v133
	v_mul_f32_e32 v20, v135, v135
	v_mul_f32_e32 v22, v128, v128
	v_mul_f32_e32 v23, v129, v129
	v_pk_fma_f32 v[18:19], v[132:133], v[132:133], v[18:19] op_sel_hi:[1,1,0]
	v_pk_fma_f32 v[20:21], v[134:135], v[134:135], v[20:21] op_sel_hi:[1,1,0]
	v_mov_b32_e32 v19, v22
	v_mov_b32_e32 v21, v23
	v_pk_add_f32 v[18:19], v[18:19], v[20:21]
	v_pk_mul_f32 v[20:21], v[126:127], v[126:127]
	v_pk_add_f32 v[16:17], v[16:17], v[18:19]
	v_pk_mul_f32 v[18:19], v[124:125], v[124:125]
	s_add_i32 s3, s3, 4
	v_pk_mov_b32 v[22:23], v[20:21], v[18:19] op_sel:[1,0]
	v_mov_b32_e32 v21, v19
	v_pk_add_f32 v[18:19], v[22:23], v[20:21]
	v_pk_mul_f32 v[20:21], v[122:123], v[122:123]
	v_pk_mul_f32 v[22:23], v[120:121], v[120:121]
	v_pk_add_f32 v[18:19], v[18:19], v[18:19] op_sel:[0,1] op_sel_hi:[1,0]
	v_pk_mov_b32 v[24:25], v[22:23], v[20:21] op_sel:[1,0]
	v_mov_b32_e32 v23, v21
	v_pk_add_f32 v[20:21], v[24:25], v[22:23]
	v_mul_f32_e32 v22, v112, v112
	v_mul_f32_e32 v23, v113, v113
	v_pk_add_f32 v[20:21], v[20:21], v[20:21] op_sel:[0,1] op_sel_hi:[1,0]
	v_mov_b32_e32 v19, v22
	v_mov_b32_e32 v21, v23
	v_pk_add_f32 v[18:19], v[18:19], v[20:21]
	v_mul_f32_e32 v20, v119, v119
	v_mul_f32_e32 v22, v117, v117
	v_mul_f32_e32 v24, v114, v114
	v_mul_f32_e32 v25, v115, v115
	v_pk_fma_f32 v[20:21], v[118:119], v[118:119], v[20:21] op_sel_hi:[1,1,0]
	v_pk_fma_f32 v[22:23], v[116:117], v[116:117], v[22:23] op_sel_hi:[1,1,0]
	v_mov_b32_e32 v21, v24
	v_mov_b32_e32 v23, v25
	v_pk_add_f32 v[20:21], v[20:21], v[22:23]
	s_add_i32 s8, s8, 8
	v_pk_add_f32 v[18:19], v[18:19], v[20:21]
	v_mov_b32_e32 v21, v16
	v_mov_b32_e32 v20, v18
	v_mov_b32_e32 v16, v19
	v_pk_add_f32 v[16:17], v[20:21], v[16:17]
	s_nop 1
	v_mov_b32_dpp v19, v17 quad_perm:[1,0,3,2] row_mask:0xf bank_mask:0xf
	s_nop 1
	v_mov_b32_dpp v18, v16 quad_perm:[1,0,3,2] row_mask:0xf bank_mask:0xf
	v_lshl_add_u64 v[76:77], v[76:77], 0, s[14:15]
	s_waitcnt lgkmcnt(0)
	v_pk_add_f32 v[16:17], v[16:17], v[18:19]
	s_nop 1
	v_mov_b32_dpp v19, v17 quad_perm:[2,3,0,1] row_mask:0xf bank_mask:0xf
	s_nop 1
	v_mov_b32_dpp v18, v16 quad_perm:[2,3,0,1] row_mask:0xf bank_mask:0xf
	s_waitcnt lgkmcnt(0)
	v_pk_add_f32 v[16:17], v[16:17], v[18:19]
	s_nop 1
	v_mov_b32_dpp v19, v17 row_half_mirror row_mask:0xf bank_mask:0xf
	s_nop 1
	v_mov_b32_dpp v18, v16 row_half_mirror row_mask:0xf bank_mask:0xf
	s_waitcnt lgkmcnt(0)
	v_pk_add_f32 v[16:17], v[16:17], v[18:19]
	s_nop 1
	v_mov_b32_dpp v19, v17 row_mirror row_mask:0xf bank_mask:0xf
	s_nop 1
	v_mov_b32_dpp v18, v16 row_mirror row_mask:0xf bank_mask:0xf
	s_waitcnt lgkmcnt(0)
	v_pk_add_f32 v[16:17], v[16:17], v[18:19]
	v_mov_b32_e32 v19, v17
	s_nop 1
	v_permlane16_swap_b32_e32 v19, v17
	v_mov_b32_e32 v18, v16
	s_nop 1
	v_permlane16_swap_b32_e32 v18, v16
	s_waitcnt lgkmcnt(0)
	v_pk_add_f32 v[16:17], v[16:17], v[18:19]
	v_mov_b32_e32 v19, v17
	s_nop 1
	v_permlane32_swap_b32_e32 v19, v17
	v_mov_b32_e32 v18, v16
	s_nop 1
	v_permlane32_swap_b32_e32 v18, v16
	s_waitcnt lgkmcnt(0)
	v_pk_add_f32 v[18:19], v[16:17], v[18:19]
	v_mov_b64_e32 v[16:17], s[12:13]
	v_pk_fma_f32 v[22:23], v[18:19], s[10:11], v[16:17] op_sel_hi:[1,0,0]
	s_nop 0
	v_mul_f32_e32 v18, 0x4b800000, v23
	v_cmp_gt_f32_e32 vcc, s26, v23
	s_nop 1
	v_cndmask_b32_e32 v18, v23, v18, vcc
	v_rsq_f32_e32 v18, v18
	v_mul_f32_e32 v23, 0x4b800000, v22
	v_mul_f32_e32 v19, 0x45800000, v18
	v_cndmask_b32_e32 v24, v18, v19, vcc
	v_pk_mul_f32 v[18:19], v[24:25], v[140:141] op_sel_hi:[0,1]
	v_pk_mul_f32 v[20:21], v[24:25], v[142:143] op_sel_hi:[0,1]
	v_pk_mul_f32 v[20:21], v[6:7], v[20:21]
	v_pk_mul_f32 v[18:19], v[4:5], v[18:19]
	global_store_dwordx4 v[78:79], v[18:21], off
	v_cmp_gt_f32_e32 vcc, s26, v22
	s_nop 0
	v_pk_mul_f32 v[18:19], v[24:25], v[136:137] op_sel_hi:[0,1]
	v_pk_mul_f32 v[20:21], v[24:25], v[138:139] op_sel_hi:[0,1]
	v_pk_mul_f32 v[20:21], v[2:3], v[20:21]
	v_pk_mul_f32 v[18:19], v[0:1], v[18:19]
	global_store_dwordx4 v[78:79], v[18:21], off offset:16
	v_cndmask_b32_e32 v22, v22, v23, vcc
	v_rsq_f32_e32 v32, v22
	v_pk_mul_f32 v[18:19], v[24:25], v[132:133] op_sel_hi:[0,1]
	v_pk_mul_f32 v[20:21], v[24:25], v[134:135] op_sel_hi:[0,1]
	v_pk_mul_f32 v[20:21], v[14:15], v[20:21]
	v_pk_mul_f32 v[18:19], v[12:13], v[18:19]
	global_store_dwordx4 v[78:79], v[18:21], off offset:2048
	v_pk_mul_f32 v[22:23], v[102:103], v[102:103]
	s_nop 0
	v_pk_mul_f32 v[18:19], v[24:25], v[130:131] op_sel_hi:[0,1]
	v_pk_mul_f32 v[20:21], v[24:25], v[128:129] op_sel_hi:[0,1]
	v_pk_mul_f32 v[24:25], v[100:101], v[100:101]
	v_pk_mul_f32 v[20:21], v[10:11], v[20:21]
	v_pk_mov_b32 v[26:27], v[24:25], v[22:23] op_sel:[1,0]
	v_mov_b32_e32 v25, v23
	v_pk_add_f32 v[22:23], v[26:27], v[24:25]
	v_pk_mul_f32 v[24:25], v[94:95], v[94:95]
	v_pk_mul_f32 v[26:27], v[92:93], v[92:93]
	v_pk_add_f32 v[22:23], v[22:23], v[22:23] op_sel:[0,1] op_sel_hi:[1,0]
	v_pk_mov_b32 v[28:29], v[26:27], v[24:25] op_sel:[1,0]
; template <int KIND, int NR> __device__ __forceinline__ void rows_block(Frame& F, const Args& a, int l, bool combine, bool moe, int m0, const f32x4 (&gm)[2][2], const f32x4 (&shv)[2][2], LAS const float* wr_l, LAS int* lcnt) {
;     ...
;         float ss = 0.f;
; #pragma unroll
;         for (int j = 0; j < 2; ++j)
; #pragma unroll
;             for (int hf = 0; hf < 2; ++hf) { const f32x4 x = v[i][j][hf]; ss += (x[0] * x[0] + x[1] * x[1]) + (x[2] * x[2] + x[3] * x[3]); }
;         ss = wsum(ss, lane);
;         const float r = rsqrtf(ss * (1.f / D) + EPS);
;         if (KIND == 2) {
; #pragma unroll
;             for (int j = 0; j < 2; ++j) { *(f32x4*)((a.out + F.zo) + (size_t)m * D + cbase + 512 * j) = v[i][j][0] * r * gm[j][0]; *(f32x4*)((a.out + F.zo) + (size_t)m * D + cbase + 512 * j + 4) = v[i][j][1] * r * gm[j][1]; }
	v_mov_b32_e32 v27, v25
	v_pk_add_f32 v[24:25], v[28:29], v[26:27]
	v_mul_f32_e32 v26, v82, v82
	v_mul_f32_e32 v27, v83, v83
	v_pk_add_f32 v[24:25], v[24:25], v[24:25] op_sel:[0,1] op_sel_hi:[1,0]
	v_mov_b32_e32 v23, v26
	v_mov_b32_e32 v25, v27
	v_pk_add_f32 v[22:23], v[22:23], v[24:25]
	v_mul_f32_e32 v24, v89, v89
	v_mul_f32_e32 v26, v91, v91
	v_mul_f32_e32 v28, v80, v80
	v_mul_f32_e32 v29, v81, v81
	v_pk_fma_f32 v[24:25], v[88:89], v[88:89], v[24:25] op_sel_hi:[1,1,0]
	v_pk_fma_f32 v[26:27], v[90:91], v[90:91], v[26:27] op_sel_hi:[1,1,0]
	v_mov_b32_e32 v25, v28
	v_mov_b32_e32 v27, v29
	v_pk_add_f32 v[24:25], v[24:25], v[26:27]
	v_pk_mul_f32 v[26:27], v[108:109], v[108:109]
	v_pk_add_f32 v[22:23], v[22:23], v[24:25]
	v_pk_mul_f32 v[24:25], v[110:111], v[110:111]
	v_pk_mul_f32 v[18:19], v[8:9], v[18:19]
	v_pk_mov_b32 v[28:29], v[26:27], v[24:25] op_sel:[1,0]
	v_mov_b32_e32 v27, v25
	v_pk_add_f32 v[24:25], v[28:29], v[26:27]
	v_pk_mul_f32 v[26:27], v[106:107], v[106:107]
	v_pk_mul_f32 v[28:29], v[104:105], v[104:105]
	v_pk_add_f32 v[24:25], v[24:25], v[24:25] op_sel:[0,1] op_sel_hi:[1,0]
	v_pk_mov_b32 v[30:31], v[28:29], v[26:27] op_sel:[1,0]
	v_mov_b32_e32 v29, v27
	v_pk_add_f32 v[26:27], v[30:31], v[28:29]
	v_mul_f32_e32 v28, v86, v86
	v_mul_f32_e32 v29, v87, v87
	v_pk_add_f32 v[26:27], v[26:27], v[26:27] op_sel:[0,1] op_sel_hi:[1,0]
	v_mov_b32_e32 v25, v28
	v_mov_b32_e32 v27, v29
	v_pk_add_f32 v[24:25], v[24:25], v[26:27]
	v_mul_f32_e32 v26, v97, v97
	v_mul_f32_e32 v28, v99, v99
	v_mul_f32_e32 v30, v84, v84
	v_mul_f32_e32 v31, v85, v85
	v_pk_fma_f32 v[26:27], v[96:97], v[96:97], v[26:27] op_sel_hi:[1,1,0]
	v_pk_fma_f32 v[28:29], v[98:99], v[98:99], v[28:29] op_sel_hi:[1,1,0]
	v_mov_b32_e32 v27, v30
	v_mov_b32_e32 v29, v31
	v_pk_add_f32 v[26:27], v[26:27], v[28:29]
	global_store_dwordx4 v[78:79], v[18:21], off offset:2064
	v_pk_add_f32 v[24:25], v[24:25], v[26:27]
	v_mov_b32_e32 v27, v22
	v_mov_b32_e32 v26, v24
	v_mov_b32_e32 v22, v25
	v_pk_add_f32 v[22:23], v[26:27], v[22:23]
	s_nop 1
	v_mov_b32_dpp v25, v23 quad_perm:[1,0,3,2] row_mask:0xf bank_mask:0xf
	s_nop 1
	v_mov_b32_dpp v24, v22 quad_perm:[1,0,3,2] row_mask:0xf bank_mask:0xf
	v_mul_f32_e32 v18, 0x45800000, v32
	v_cndmask_b32_e32 v26, v32, v18, vcc
	v_pk_mul_f32 v[18:19], v[26:27], v[126:127] op_sel_hi:[0,1]
	v_pk_mul_f32 v[20:21], v[26:27], v[124:125] op_sel_hi:[0,1]
	s_waitcnt lgkmcnt(0)
	v_pk_add_f32 v[22:23], v[22:23], v[24:25]
	s_nop 1
	v_mov_b32_dpp v25, v23 quad_perm:[2,3,0,1] row_mask:0xf bank_mask:0xf
	s_nop 1
	v_mov_b32_dpp v24, v22 quad_perm:[2,3,0,1] row_mask:0xf bank_mask:0xf
	v_pk_mul_f32 v[20:21], v[6:7], v[20:21]
	v_pk_mul_f32 v[18:19], v[4:5], v[18:19]
	v_lshl_add_u64 v[28:29], v[72:73], 0, s[0:1]
	global_store_dwordx4 v[28:29], v[18:21], off
	s_waitcnt lgkmcnt(0)
	v_pk_add_f32 v[22:23], v[22:23], v[24:25]
	s_nop 1
	v_mov_b32_dpp v25, v23 row_half_mirror row_mask:0xf bank_mask:0xf
	s_nop 1
	v_mov_b32_dpp v24, v22 row_half_mirror row_mask:0xf bank_mask:0xf
	v_pk_mul_f32 v[18:19], v[26:27], v[120:121] op_sel_hi:[0,1]
	v_pk_mul_f32 v[20:21], v[26:27], v[122:123] op_sel_hi:[0,1]
	v_pk_mul_f32 v[20:21], v[2:3], v[20:21]
	v_pk_mul_f32 v[18:19], v[0:1], v[18:19]
	s_waitcnt lgkmcnt(0)
	v_pk_add_f32 v[22:23], v[22:23], v[24:25]
	s_nop 1
	v_mov_b32_dpp v25, v23 row_mirror row_mask:0xf bank_mask:0xf
	s_nop 1
	v_mov_b32_dpp v24, v22 row_mirror row_mask:0xf bank_mask:0xf
	global_store_dwordx4 v[28:29], v[18:21], off offset:16
	s_lshl_b64 s[0:1], s[20:21], 12
	v_lshl_add_u64 v[78:79], v[78:79], 0, s[16:17]
	v_pk_mul_f32 v[18:19], v[26:27], v[118:119] op_sel_hi:[0,1]
	s_waitcnt lgkmcnt(0)
; template <int KIND, int NR> __device__ __forceinline__ void rows_block(Frame& F, const Args& a, int l, bool combine, bool moe, int m0, const f32x4 (&gm)[2][2], const f32x4 (&shv)[2][2], LAS const float* wr_l, LAS int* lcnt) {
;     ...
;         float ss = 0.f;
; #pragma unroll
;         for (int j = 0; j < 2; ++j)
; #pragma unroll
;             for (int hf = 0; hf < 2; ++hf) { const f32x4 x = v[i][j][hf]; ss += (x[0] * x[0] + x[1] * x[1]) + (x[2] * x[2] + x[3] * x[3]); }
;         ss = wsum(ss, lane);
;         const float r = rsqrtf(ss * (1.f / D) + EPS);
;         if (KIND == 2) {
; #pragma unroll
;             for (int j = 0; j < 2; ++j) { *(f32x4*)((a.out + F.zo) + (size_t)m * D + cbase + 512 * j) = v[i][j][0] * r * gm[j][0]; *(f32x4*)((a.out + F.zo) + (size_t)m * D + cbase + 512 * j + 4) = v[i][j][1] * r * gm[j][1]; }
	v_pk_add_f32 v[22:23], v[22:23], v[24:25]
	v_mov_b32_e32 v25, v23
	s_nop 1
	v_permlane16_swap_b32_e32 v25, v23
	v_mov_b32_e32 v24, v22
	s_nop 1
	v_permlane16_swap_b32_e32 v24, v22
	v_pk_mul_f32 v[20:21], v[26:27], v[116:117] op_sel_hi:[0,1]
	v_pk_mul_f32 v[20:21], v[14:15], v[20:21]
	v_pk_mul_f32 v[18:19], v[12:13], v[18:19]
	global_store_dwordx4 v[28:29], v[18:21], off offset:2048
	s_waitcnt lgkmcnt(0)
	v_pk_add_f32 v[22:23], v[22:23], v[24:25]
	v_mov_b32_e32 v25, v23
	s_nop 1
	v_permlane32_swap_b32_e32 v25, v23
	v_mov_b32_e32 v24, v22
	s_nop 1
	v_permlane32_swap_b32_e32 v24, v22
	v_pk_mul_f32 v[18:19], v[26:27], v[112:113] op_sel_hi:[0,1]
	v_pk_mul_f32 v[20:21], v[26:27], v[114:115] op_sel_hi:[0,1]
	v_pk_mul_f32 v[20:21], v[10:11], v[20:21]
	v_pk_mul_f32 v[18:19], v[8:9], v[18:19]
	s_waitcnt lgkmcnt(0)
	v_pk_add_f32 v[22:23], v[22:23], v[24:25]
	global_store_dwordx4 v[28:29], v[18:21], off offset:2064
	v_pk_fma_f32 v[22:23], v[22:23], s[10:11], v[16:17] op_sel_hi:[1,0,0]
	s_nop 0
	v_mul_f32_e32 v16, 0x4b800000, v23
	v_cmp_gt_f32_e32 vcc, s26, v23
	v_lshl_add_u64 v[20:21], v[72:73], 0, s[0:1]
	s_lshl_b64 s[0:1], s[22:23], 12
	v_cndmask_b32_e32 v16, v23, v16, vcc
	v_rsq_f32_e32 v16, v16
	v_mul_f32_e32 v23, 0x4b800000, v22
	s_cmp_lt_i32 s3, s11
	v_mul_f32_e32 v17, 0x45800000, v16
	v_cndmask_b32_e32 v24, v16, v17, vcc
	v_pk_mul_f32 v[16:17], v[24:25], v[100:101] op_sel_hi:[0,1]
	v_pk_mul_f32 v[18:19], v[24:25], v[102:103] op_sel_hi:[0,1]
	v_pk_mul_f32 v[18:19], v[6:7], v[18:19]
	v_pk_mul_f32 v[16:17], v[4:5], v[16:17]
	global_store_dwordx4 v[20:21], v[16:19], off
	v_cmp_gt_f32_e32 vcc, s26, v22
	s_nop 0
	v_pk_mul_f32 v[16:17], v[24:25], v[92:93] op_sel_hi:[0,1]
	v_pk_mul_f32 v[18:19], v[24:25], v[94:95] op_sel_hi:[0,1]
	v_pk_mul_f32 v[18:19], v[2:3], v[18:19]
	v_pk_mul_f32 v[16:17], v[0:1], v[16:17]
	v_cndmask_b32_e32 v22, v22, v23, vcc
	global_store_dwordx4 v[20:21], v[16:19], off offset:16
	v_rsq_f32_e32 v22, v22
	s_nop 0
	v_pk_mul_f32 v[16:17], v[24:25], v[88:89] op_sel_hi:[0,1]
	v_pk_mul_f32 v[18:19], v[24:25], v[90:91] op_sel_hi:[0,1]
	v_pk_mul_f32 v[18:19], v[14:15], v[18:19]
	v_pk_mul_f32 v[16:17], v[12:13], v[16:17]
	global_store_dwordx4 v[20:21], v[16:19], off offset:2048
	s_nop 1
	v_pk_mul_f32 v[16:17], v[24:25], v[82:83] op_sel_hi:[0,1]
	v_pk_mul_f32 v[18:19], v[24:25], v[80:81] op_sel_hi:[0,1]
	v_pk_mul_f32 v[18:19], v[10:11], v[18:19]
	v_pk_mul_f32 v[16:17], v[8:9], v[16:17]
	global_store_dwordx4 v[20:21], v[16:19], off offset:2064
	s_nop 1
	v_mul_f32_e32 v16, 0x45800000, v22
	v_cndmask_b32_e32 v20, v22, v16, vcc
	v_pk_mul_f32 v[16:17], v[20:21], v[108:109] op_sel_hi:[0,1]
	v_pk_mul_f32 v[18:19], v[20:21], v[110:111] op_sel_hi:[0,1]
	v_pk_mul_f32 v[18:19], v[6:7], v[18:19]
	v_pk_mul_f32 v[16:17], v[4:5], v[16:17]
	v_lshl_add_u64 v[22:23], v[72:73], 0, s[0:1]
	global_store_dwordx4 v[22:23], v[16:19], off
	s_nop 1
	v_pk_mul_f32 v[16:17], v[20:21], v[104:105] op_sel_hi:[0,1]
	v_pk_mul_f32 v[18:19], v[20:21], v[106:107] op_sel_hi:[0,1]
	v_pk_mul_f32 v[18:19], v[2:3], v[18:19]
	v_pk_mul_f32 v[16:17], v[0:1], v[16:17]
	global_store_dwordx4 v[22:23], v[16:19], off offset:16
	s_nop 1
	v_pk_mul_f32 v[16:17], v[20:21], v[96:97] op_sel_hi:[0,1]
	v_pk_mul_f32 v[18:19], v[20:21], v[98:99] op_sel_hi:[0,1]
	v_pk_mul_f32 v[18:19], v[14:15], v[18:19]
	v_pk_mul_f32 v[16:17], v[12:13], v[16:17]
	global_store_dwordx4 v[22:23], v[16:19], off offset:2048
	s_nop 1
	v_pk_mul_f32 v[16:17], v[20:21], v[86:87] op_sel_hi:[0,1]
	v_pk_mul_f32 v[18:19], v[20:21], v[84:85] op_sel_hi:[0,1]
	v_pk_mul_f32 v[18:19], v[10:11], v[18:19]
	v_pk_mul_f32 v[16:17], v[8:9], v[16:17]
	global_store_dwordx4 v[22:23], v[16:19], off offset:2064
	s_cbranch_scc0 .LBB13_1645
